# attention epilogue: DPP quad_perm lane swap + batched stores instead of 128 serialized ds_bpermute round trips (on top of v22)
# speedup vs baseline: 1.0242x; 1.0017x over previous
; __device__ __forceinline__ int crow(int r, int hi) { return (r & 3) + 8 * (r >> 2) + 4 * hi; }
; __device__ __forceinline__ void block(const Blk& B, char* lds, A3_LAS unsigned char* ldsl, const int tid) {
;     ...
;     { auto rr = __builtin_amdgcn_permlane32_swap(__float_as_uint(l_reg), __float_as_uint(l_reg), false, false); l_reg = __uint_as_float(rr[0]) + __uint_as_float(rr[1]); }
;     if (hi == 0) sc_l[32 + r32] = l_reg;
;     asm volatile("s_waitcnt lgkmcnt(0)" ::: "memory");
;     float rli[16];
; #pragma unroll
;     for (int r = 0; r < 16; ++r) rli[r] = __builtin_amdgcn_rcpf(sc_l[32 + attn::crow(r, hi)]);
;     abf* Ow = B.O + (size_t)(wid * 32) * LDO;
; #pragma unroll
;     for (int r = 0; r < 16; ++r) { const int orow = attn::crow(r, hi);
; #pragma unroll
;         for (int d0 = 0; d0 < 8; ++d0) { const float v = o[d0][r] * rli[r]; const float vn = __shfl_xor(v, 1);
;             if ((r32 & 1) == 0) *(unsigned*)(Ow + (size_t)orow * LDO + d0 * 32 + r32) = attn::cvtpk(v, vn); } }
.LBB0_338:
	v_mov_b32_e32 v0, v146
	s_nop 1
	v_permlane32_swap_b32_e32 v146, v0
	s_and_saveexec_b64 s[58:59], s[2:3]
	v_add_f32_e32 v0, v146, v0
	ds_write_b32 v204, v0 offset:128
	s_or_b64 exec, exec, s[58:59]
	s_waitcnt lgkmcnt(0)
	ds_read_b128 v[142:145], v203 offset:128
	ds_read_b128 v[138:141], v203 offset:160
	ds_read_b128 v[134:137], v203 offset:192
	ds_read_b128 v[130:133], v203 offset:224
	s_lshl_b32 s2, s6, 21
	s_add_u32 s4, s67, s2
	s_addc_u32 s5, s24, 0
	s_ashr_i32 s57, s56, 31
	s_lshl_b64 s[2:3], s[56:57], 13
	s_add_u32 s4, s4, s2
	s_addc_u32 s5, s5, s3
	v_lshlrev_b32_e32 v0, 1, v196
	v_lshl_add_u64 v[146:147], s[4:5], 0, v[0:1]
	v_lshlrev_b32_e32 v0, 15, v198
	v_lshl_add_u64 v[146:147], v[146:147], 0, v[0:1]
	v_and_b32_e32 v0, 1, v197
	v_cmp_eq_u32_e64 s[2:3], 0, v0
	s_waitcnt lgkmcnt(0)
	v_rcp_f32_e32 v142, v142
	v_rcp_f32_e32 v143, v143
	v_rcp_f32_e32 v144, v144
	v_rcp_f32_e32 v145, v145
	v_rcp_f32_e32 v138, v138
	v_rcp_f32_e32 v139, v139
	v_rcp_f32_e32 v140, v140
	v_rcp_f32_e32 v141, v141
	v_rcp_f32_e32 v134, v134
	v_rcp_f32_e32 v135, v135
	v_rcp_f32_e32 v136, v136
	v_rcp_f32_e32 v137, v137
	v_rcp_f32_e32 v130, v130
	v_rcp_f32_e32 v131, v131
	v_rcp_f32_e32 v132, v132
	v_rcp_f32_e32 v133, v133
	s_nop 0
	v_mul_f32_e32 v212, v114, v142
	v_mul_f32_e32 v213, v98, v142
	v_mul_f32_e32 v214, v82, v142
	v_mul_f32_e32 v215, v66, v142
	v_mul_f32_e32 v216, v50, v142
	v_mul_f32_e32 v217, v34, v142
	v_mul_f32_e32 v218, v18, v142
	v_mul_f32_e32 v219, v2, v142
	v_mov_b32_dpp v220, v212 quad_perm:[1,0,3,2] row_mask:0xf bank_mask:0xf
	v_mov_b32_dpp v221, v213 quad_perm:[1,0,3,2] row_mask:0xf bank_mask:0xf
	v_mov_b32_dpp v222, v214 quad_perm:[1,0,3,2] row_mask:0xf bank_mask:0xf
	v_mov_b32_dpp v223, v215 quad_perm:[1,0,3,2] row_mask:0xf bank_mask:0xf
	v_mov_b32_dpp v224, v216 quad_perm:[1,0,3,2] row_mask:0xf bank_mask:0xf
	v_mov_b32_dpp v225, v217 quad_perm:[1,0,3,2] row_mask:0xf bank_mask:0xf
	v_mov_b32_dpp v226, v218 quad_perm:[1,0,3,2] row_mask:0xf bank_mask:0xf
	v_mov_b32_dpp v227, v219 quad_perm:[1,0,3,2] row_mask:0xf bank_mask:0xf
	v_cvt_pk_bf16_f32 v212, v212, v220
	v_cvt_pk_bf16_f32 v213, v213, v221
	v_cvt_pk_bf16_f32 v214, v214, v222
	v_cvt_pk_bf16_f32 v215, v215, v223
	v_cvt_pk_bf16_f32 v216, v216, v224
	v_cvt_pk_bf16_f32 v217, v217, v225
	v_cvt_pk_bf16_f32 v218, v218, v226
	v_cvt_pk_bf16_f32 v219, v219, v227
	s_mov_b64 exec, s[2:3]
	global_store_dword v[146:147], v212, off
	global_store_dword v[146:147], v213, off offset:64
	global_store_dword v[146:147], v214, off offset:128
	global_store_dword v[146:147], v215, off offset:192
	global_store_dword v[146:147], v216, off offset:256
	global_store_dword v[146:147], v217, off offset:320
	global_store_dword v[146:147], v218, off offset:384
	global_store_dword v[146:147], v219, off offset:448
	s_mov_b64 exec, -1
	s_mov_b64 s[60:61], 0x2000
	v_lshl_add_u64 v[228:229], v[146:147], 0, s[60:61]
	v_mul_f32_e32 v230, v115, v143
	v_mul_f32_e32 v231, v99, v143
	v_mul_f32_e32 v232, v83, v143
	v_mul_f32_e32 v233, v67, v143
	v_mul_f32_e32 v234, v51, v143
	v_mul_f32_e32 v235, v35, v143
	v_mul_f32_e32 v236, v19, v143
	v_mul_f32_e32 v237, v3, v143
	v_mov_b32_dpp v238, v230 quad_perm:[1,0,3,2] row_mask:0xf bank_mask:0xf
	v_mov_b32_dpp v239, v231 quad_perm:[1,0,3,2] row_mask:0xf bank_mask:0xf
	v_mov_b32_dpp v240, v232 quad_perm:[1,0,3,2] row_mask:0xf bank_mask:0xf
	v_mov_b32_dpp v241, v233 quad_perm:[1,0,3,2] row_mask:0xf bank_mask:0xf
	v_mov_b32_dpp v242, v234 quad_perm:[1,0,3,2] row_mask:0xf bank_mask:0xf
	v_mov_b32_dpp v243, v235 quad_perm:[1,0,3,2] row_mask:0xf bank_mask:0xf
	v_mov_b32_dpp v244, v236 quad_perm:[1,0,3,2] row_mask:0xf bank_mask:0xf
	v_mov_b32_dpp v245, v237 quad_perm:[1,0,3,2] row_mask:0xf bank_mask:0xf
	v_cvt_pk_bf16_f32 v230, v230, v238
	v_cvt_pk_bf16_f32 v231, v231, v239
	v_cvt_pk_bf16_f32 v232, v232, v240
	v_cvt_pk_bf16_f32 v233, v233, v241
	v_cvt_pk_bf16_f32 v234, v234, v242
	v_cvt_pk_bf16_f32 v235, v235, v243
	v_cvt_pk_bf16_f32 v236, v236, v244
	v_cvt_pk_bf16_f32 v237, v237, v245
	s_mov_b64 exec, s[2:3]
	global_store_dword v[228:229], v230, off
	global_store_dword v[228:229], v231, off offset:64
	global_store_dword v[228:229], v232, off offset:128
	global_store_dword v[228:229], v233, off offset:192
	global_store_dword v[228:229], v234, off offset:256
	global_store_dword v[228:229], v235, off offset:320
	global_store_dword v[228:229], v236, off offset:384
	global_store_dword v[228:229], v237, off offset:448
	s_mov_b64 exec, -1
	s_mov_b64 s[60:61], 0x4000
	v_lshl_add_u64 v[228:229], v[146:147], 0, s[60:61]
	v_mul_f32_e32 v212, v116, v144
	v_mul_f32_e32 v213, v100, v144
	v_mul_f32_e32 v214, v84, v144
	v_mul_f32_e32 v215, v68, v144
	v_mul_f32_e32 v216, v52, v144
	v_mul_f32_e32 v217, v36, v144
	v_mul_f32_e32 v218, v20, v144
	v_mul_f32_e32 v219, v4, v144
	v_mov_b32_dpp v220, v212 quad_perm:[1,0,3,2] row_mask:0xf bank_mask:0xf
	v_mov_b32_dpp v221, v213 quad_perm:[1,0,3,2] row_mask:0xf bank_mask:0xf
	v_mov_b32_dpp v222, v214 quad_perm:[1,0,3,2] row_mask:0xf bank_mask:0xf
	v_mov_b32_dpp v223, v215 quad_perm:[1,0,3,2] row_mask:0xf bank_mask:0xf
	v_mov_b32_dpp v224, v216 quad_perm:[1,0,3,2] row_mask:0xf bank_mask:0xf
	v_mov_b32_dpp v225, v217 quad_perm:[1,0,3,2] row_mask:0xf bank_mask:0xf
	v_mov_b32_dpp v226, v218 quad_perm:[1,0,3,2] row_mask:0xf bank_mask:0xf
	v_mov_b32_dpp v227, v219 quad_perm:[1,0,3,2] row_mask:0xf bank_mask:0xf
	v_cvt_pk_bf16_f32 v212, v212, v220
	v_cvt_pk_bf16_f32 v213, v213, v221
	v_cvt_pk_bf16_f32 v214, v214, v222
	v_cvt_pk_bf16_f32 v215, v215, v223
	v_cvt_pk_bf16_f32 v216, v216, v224
	v_cvt_pk_bf16_f32 v217, v217, v225
	v_cvt_pk_bf16_f32 v218, v218, v226
; __device__ __forceinline__ int crow(int r, int hi) { return (r & 3) + 8 * (r >> 2) + 4 * hi; }
; __device__ __forceinline__ void block(const Blk& B, char* lds, A3_LAS unsigned char* ldsl, const int tid) {
;     ...
;     for (int r = 0; r < 16; ++r) { const int orow = attn::crow(r, hi);
; #pragma unroll
;         for (int d0 = 0; d0 < 8; ++d0) { const float v = o[d0][r] * rli[r]; const float vn = __shfl_xor(v, 1);
;             if ((r32 & 1) == 0) *(unsigned*)(Ow + (size_t)orow * LDO + d0 * 32 + r32) = attn::cvtpk(v, vn); } }
	v_cvt_pk_bf16_f32 v219, v219, v227
	s_mov_b64 exec, s[2:3]
	global_store_dword v[228:229], v212, off
	global_store_dword v[228:229], v213, off offset:64
	global_store_dword v[228:229], v214, off offset:128
	global_store_dword v[228:229], v215, off offset:192
	global_store_dword v[228:229], v216, off offset:256
	global_store_dword v[228:229], v217, off offset:320
	global_store_dword v[228:229], v218, off offset:384
	global_store_dword v[228:229], v219, off offset:448
	s_mov_b64 exec, -1
	s_mov_b64 s[60:61], 0x6000
	v_lshl_add_u64 v[228:229], v[146:147], 0, s[60:61]
	v_mul_f32_e32 v230, v117, v145
	v_mul_f32_e32 v231, v101, v145
	v_mul_f32_e32 v232, v85, v145
	v_mul_f32_e32 v233, v69, v145
	v_mul_f32_e32 v234, v53, v145
	v_mul_f32_e32 v235, v37, v145
	v_mul_f32_e32 v236, v21, v145
	v_mul_f32_e32 v237, v5, v145
	v_mov_b32_dpp v238, v230 quad_perm:[1,0,3,2] row_mask:0xf bank_mask:0xf
	v_mov_b32_dpp v239, v231 quad_perm:[1,0,3,2] row_mask:0xf bank_mask:0xf
	v_mov_b32_dpp v240, v232 quad_perm:[1,0,3,2] row_mask:0xf bank_mask:0xf
	v_mov_b32_dpp v241, v233 quad_perm:[1,0,3,2] row_mask:0xf bank_mask:0xf
	v_mov_b32_dpp v242, v234 quad_perm:[1,0,3,2] row_mask:0xf bank_mask:0xf
	v_mov_b32_dpp v243, v235 quad_perm:[1,0,3,2] row_mask:0xf bank_mask:0xf
	v_mov_b32_dpp v244, v236 quad_perm:[1,0,3,2] row_mask:0xf bank_mask:0xf
	v_mov_b32_dpp v245, v237 quad_perm:[1,0,3,2] row_mask:0xf bank_mask:0xf
	v_cvt_pk_bf16_f32 v230, v230, v238
	v_cvt_pk_bf16_f32 v231, v231, v239
	v_cvt_pk_bf16_f32 v232, v232, v240
	v_cvt_pk_bf16_f32 v233, v233, v241
	v_cvt_pk_bf16_f32 v234, v234, v242
	v_cvt_pk_bf16_f32 v235, v235, v243
	v_cvt_pk_bf16_f32 v236, v236, v244
	v_cvt_pk_bf16_f32 v237, v237, v245
	s_mov_b64 exec, s[2:3]
	global_store_dword v[228:229], v230, off
	global_store_dword v[228:229], v231, off offset:64
	global_store_dword v[228:229], v232, off offset:128
	global_store_dword v[228:229], v233, off offset:192
	global_store_dword v[228:229], v234, off offset:256
	global_store_dword v[228:229], v235, off offset:320
	global_store_dword v[228:229], v236, off offset:384
	global_store_dword v[228:229], v237, off offset:448
	s_mov_b64 exec, -1
	s_mov_b64 s[60:61], 0x10000
	v_lshl_add_u64 v[228:229], v[146:147], 0, s[60:61]
	v_mul_f32_e32 v212, v118, v138
	v_mul_f32_e32 v213, v102, v138
	v_mul_f32_e32 v214, v86, v138
	v_mul_f32_e32 v215, v70, v138
	v_mul_f32_e32 v216, v54, v138
	v_mul_f32_e32 v217, v38, v138
	v_mul_f32_e32 v218, v22, v138
	v_mul_f32_e32 v219, v6, v138
	v_mov_b32_dpp v220, v212 quad_perm:[1,0,3,2] row_mask:0xf bank_mask:0xf
	v_mov_b32_dpp v221, v213 quad_perm:[1,0,3,2] row_mask:0xf bank_mask:0xf
	v_mov_b32_dpp v222, v214 quad_perm:[1,0,3,2] row_mask:0xf bank_mask:0xf
	v_mov_b32_dpp v223, v215 quad_perm:[1,0,3,2] row_mask:0xf bank_mask:0xf
	v_mov_b32_dpp v224, v216 quad_perm:[1,0,3,2] row_mask:0xf bank_mask:0xf
	v_mov_b32_dpp v225, v217 quad_perm:[1,0,3,2] row_mask:0xf bank_mask:0xf
	v_mov_b32_dpp v226, v218 quad_perm:[1,0,3,2] row_mask:0xf bank_mask:0xf
	v_mov_b32_dpp v227, v219 quad_perm:[1,0,3,2] row_mask:0xf bank_mask:0xf
	v_cvt_pk_bf16_f32 v212, v212, v220
	v_cvt_pk_bf16_f32 v213, v213, v221
	v_cvt_pk_bf16_f32 v214, v214, v222
	v_cvt_pk_bf16_f32 v215, v215, v223
	v_cvt_pk_bf16_f32 v216, v216, v224
	v_cvt_pk_bf16_f32 v217, v217, v225
	v_cvt_pk_bf16_f32 v218, v218, v226
	v_cvt_pk_bf16_f32 v219, v219, v227
	s_mov_b64 exec, s[2:3]
	global_store_dword v[228:229], v212, off
	global_store_dword v[228:229], v213, off offset:64
	global_store_dword v[228:229], v214, off offset:128
	global_store_dword v[228:229], v215, off offset:192
	global_store_dword v[228:229], v216, off offset:256
	global_store_dword v[228:229], v217, off offset:320
	global_store_dword v[228:229], v218, off offset:384
	global_store_dword v[228:229], v219, off offset:448
	s_mov_b64 exec, -1
	s_mov_b64 s[60:61], 0x12000
	v_lshl_add_u64 v[228:229], v[146:147], 0, s[60:61]
	v_mul_f32_e32 v230, v119, v139
	v_mul_f32_e32 v231, v103, v139
	v_mul_f32_e32 v232, v87, v139
	v_mul_f32_e32 v233, v71, v139
	v_mul_f32_e32 v234, v55, v139
	v_mul_f32_e32 v235, v39, v139
	v_mul_f32_e32 v236, v23, v139
	v_mul_f32_e32 v237, v7, v139
	v_mov_b32_dpp v238, v230 quad_perm:[1,0,3,2] row_mask:0xf bank_mask:0xf
	v_mov_b32_dpp v239, v231 quad_perm:[1,0,3,2] row_mask:0xf bank_mask:0xf
	v_mov_b32_dpp v240, v232 quad_perm:[1,0,3,2] row_mask:0xf bank_mask:0xf
	v_mov_b32_dpp v241, v233 quad_perm:[1,0,3,2] row_mask:0xf bank_mask:0xf
	v_mov_b32_dpp v242, v234 quad_perm:[1,0,3,2] row_mask:0xf bank_mask:0xf
	v_mov_b32_dpp v243, v235 quad_perm:[1,0,3,2] row_mask:0xf bank_mask:0xf
	v_mov_b32_dpp v244, v236 quad_perm:[1,0,3,2] row_mask:0xf bank_mask:0xf
	v_mov_b32_dpp v245, v237 quad_perm:[1,0,3,2] row_mask:0xf bank_mask:0xf
	v_cvt_pk_bf16_f32 v230, v230, v238
	v_cvt_pk_bf16_f32 v231, v231, v239
	v_cvt_pk_bf16_f32 v232, v232, v240
	v_cvt_pk_bf16_f32 v233, v233, v241
	v_cvt_pk_bf16_f32 v234, v234, v242
	v_cvt_pk_bf16_f32 v235, v235, v243
	v_cvt_pk_bf16_f32 v236, v236, v244
	v_cvt_pk_bf16_f32 v237, v237, v245
	s_mov_b64 exec, s[2:3]
	global_store_dword v[228:229], v230, off
	global_store_dword v[228:229], v231, off offset:64
	global_store_dword v[228:229], v232, off offset:128
	global_store_dword v[228:229], v233, off offset:192
	global_store_dword v[228:229], v234, off offset:256
	global_store_dword v[228:229], v235, off offset:320
	global_store_dword v[228:229], v236, off offset:384
	global_store_dword v[228:229], v237, off offset:448
	s_mov_b64 exec, -1
	s_mov_b64 s[60:61], 0x14000
	v_lshl_add_u64 v[228:229], v[146:147], 0, s[60:61]
	v_mul_f32_e32 v212, v120, v140
	v_mul_f32_e32 v213, v104, v140
	v_mul_f32_e32 v214, v88, v140
; __device__ __forceinline__ int crow(int r, int hi) { return (r & 3) + 8 * (r >> 2) + 4 * hi; }
; __device__ __forceinline__ void block(const Blk& B, char* lds, A3_LAS unsigned char* ldsl, const int tid) {
;     ...
;     for (int r = 0; r < 16; ++r) { const int orow = attn::crow(r, hi);
; #pragma unroll
;         for (int d0 = 0; d0 < 8; ++d0) { const float v = o[d0][r] * rli[r]; const float vn = __shfl_xor(v, 1);
;             if ((r32 & 1) == 0) *(unsigned*)(Ow + (size_t)orow * LDO + d0 * 32 + r32) = attn::cvtpk(v, vn); } }
	v_mul_f32_e32 v215, v72, v140
	v_mul_f32_e32 v216, v56, v140
	v_mul_f32_e32 v217, v40, v140
	v_mul_f32_e32 v218, v24, v140
	v_mul_f32_e32 v219, v8, v140
	v_mov_b32_dpp v220, v212 quad_perm:[1,0,3,2] row_mask:0xf bank_mask:0xf
	v_mov_b32_dpp v221, v213 quad_perm:[1,0,3,2] row_mask:0xf bank_mask:0xf
	v_mov_b32_dpp v222, v214 quad_perm:[1,0,3,2] row_mask:0xf bank_mask:0xf
	v_mov_b32_dpp v223, v215 quad_perm:[1,0,3,2] row_mask:0xf bank_mask:0xf
	v_mov_b32_dpp v224, v216 quad_perm:[1,0,3,2] row_mask:0xf bank_mask:0xf
	v_mov_b32_dpp v225, v217 quad_perm:[1,0,3,2] row_mask:0xf bank_mask:0xf
	v_mov_b32_dpp v226, v218 quad_perm:[1,0,3,2] row_mask:0xf bank_mask:0xf
	v_mov_b32_dpp v227, v219 quad_perm:[1,0,3,2] row_mask:0xf bank_mask:0xf
	v_cvt_pk_bf16_f32 v212, v212, v220
	v_cvt_pk_bf16_f32 v213, v213, v221
	v_cvt_pk_bf16_f32 v214, v214, v222
	v_cvt_pk_bf16_f32 v215, v215, v223
	v_cvt_pk_bf16_f32 v216, v216, v224
	v_cvt_pk_bf16_f32 v217, v217, v225
	v_cvt_pk_bf16_f32 v218, v218, v226
	v_cvt_pk_bf16_f32 v219, v219, v227
	s_mov_b64 exec, s[2:3]
	global_store_dword v[228:229], v212, off
	global_store_dword v[228:229], v213, off offset:64
	global_store_dword v[228:229], v214, off offset:128
	global_store_dword v[228:229], v215, off offset:192
	global_store_dword v[228:229], v216, off offset:256
	global_store_dword v[228:229], v217, off offset:320
	global_store_dword v[228:229], v218, off offset:384
	global_store_dword v[228:229], v219, off offset:448
	s_mov_b64 exec, -1
	s_mov_b64 s[60:61], 0x16000
	v_lshl_add_u64 v[228:229], v[146:147], 0, s[60:61]
	v_mul_f32_e32 v230, v121, v141
	v_mul_f32_e32 v231, v105, v141
	v_mul_f32_e32 v232, v89, v141
	v_mul_f32_e32 v233, v73, v141
	v_mul_f32_e32 v234, v57, v141
	v_mul_f32_e32 v235, v41, v141
	v_mul_f32_e32 v236, v25, v141
	v_mul_f32_e32 v237, v9, v141
	v_mov_b32_dpp v238, v230 quad_perm:[1,0,3,2] row_mask:0xf bank_mask:0xf
	v_mov_b32_dpp v239, v231 quad_perm:[1,0,3,2] row_mask:0xf bank_mask:0xf
	v_mov_b32_dpp v240, v232 quad_perm:[1,0,3,2] row_mask:0xf bank_mask:0xf
	v_mov_b32_dpp v241, v233 quad_perm:[1,0,3,2] row_mask:0xf bank_mask:0xf
	v_mov_b32_dpp v242, v234 quad_perm:[1,0,3,2] row_mask:0xf bank_mask:0xf
	v_mov_b32_dpp v243, v235 quad_perm:[1,0,3,2] row_mask:0xf bank_mask:0xf
	v_mov_b32_dpp v244, v236 quad_perm:[1,0,3,2] row_mask:0xf bank_mask:0xf
	v_mov_b32_dpp v245, v237 quad_perm:[1,0,3,2] row_mask:0xf bank_mask:0xf
	v_cvt_pk_bf16_f32 v230, v230, v238
	v_cvt_pk_bf16_f32 v231, v231, v239
	v_cvt_pk_bf16_f32 v232, v232, v240
	v_cvt_pk_bf16_f32 v233, v233, v241
	v_cvt_pk_bf16_f32 v234, v234, v242
	v_cvt_pk_bf16_f32 v235, v235, v243
	v_cvt_pk_bf16_f32 v236, v236, v244
	v_cvt_pk_bf16_f32 v237, v237, v245
	s_mov_b64 exec, s[2:3]
	global_store_dword v[228:229], v230, off
	global_store_dword v[228:229], v231, off offset:64
	global_store_dword v[228:229], v232, off offset:128
	global_store_dword v[228:229], v233, off offset:192
	global_store_dword v[228:229], v234, off offset:256
	global_store_dword v[228:229], v235, off offset:320
	global_store_dword v[228:229], v236, off offset:384
	global_store_dword v[228:229], v237, off offset:448
	s_mov_b64 exec, -1
	s_mov_b64 s[60:61], 0x20000
	v_lshl_add_u64 v[228:229], v[146:147], 0, s[60:61]
	v_mul_f32_e32 v212, v122, v134
	v_mul_f32_e32 v213, v106, v134
	v_mul_f32_e32 v214, v90, v134
	v_mul_f32_e32 v215, v74, v134
	v_mul_f32_e32 v216, v58, v134
	v_mul_f32_e32 v217, v42, v134
	v_mul_f32_e32 v218, v26, v134
	v_mul_f32_e32 v219, v10, v134
	v_mov_b32_dpp v220, v212 quad_perm:[1,0,3,2] row_mask:0xf bank_mask:0xf
	v_mov_b32_dpp v221, v213 quad_perm:[1,0,3,2] row_mask:0xf bank_mask:0xf
	v_mov_b32_dpp v222, v214 quad_perm:[1,0,3,2] row_mask:0xf bank_mask:0xf
	v_mov_b32_dpp v223, v215 quad_perm:[1,0,3,2] row_mask:0xf bank_mask:0xf
	v_mov_b32_dpp v224, v216 quad_perm:[1,0,3,2] row_mask:0xf bank_mask:0xf
	v_mov_b32_dpp v225, v217 quad_perm:[1,0,3,2] row_mask:0xf bank_mask:0xf
	v_mov_b32_dpp v226, v218 quad_perm:[1,0,3,2] row_mask:0xf bank_mask:0xf
	v_mov_b32_dpp v227, v219 quad_perm:[1,0,3,2] row_mask:0xf bank_mask:0xf
	v_cvt_pk_bf16_f32 v212, v212, v220
	v_cvt_pk_bf16_f32 v213, v213, v221
	v_cvt_pk_bf16_f32 v214, v214, v222
	v_cvt_pk_bf16_f32 v215, v215, v223
	v_cvt_pk_bf16_f32 v216, v216, v224
	v_cvt_pk_bf16_f32 v217, v217, v225
	v_cvt_pk_bf16_f32 v218, v218, v226
	v_cvt_pk_bf16_f32 v219, v219, v227
	s_mov_b64 exec, s[2:3]
	global_store_dword v[228:229], v212, off
	global_store_dword v[228:229], v213, off offset:64
	global_store_dword v[228:229], v214, off offset:128
	global_store_dword v[228:229], v215, off offset:192
	global_store_dword v[228:229], v216, off offset:256
	global_store_dword v[228:229], v217, off offset:320
	global_store_dword v[228:229], v218, off offset:384
	global_store_dword v[228:229], v219, off offset:448
	s_mov_b64 exec, -1
	s_mov_b64 s[60:61], 0x22000
	v_lshl_add_u64 v[228:229], v[146:147], 0, s[60:61]
	v_mul_f32_e32 v230, v123, v135
	v_mul_f32_e32 v231, v107, v135
	v_mul_f32_e32 v232, v91, v135
	v_mul_f32_e32 v233, v75, v135
	v_mul_f32_e32 v234, v59, v135
	v_mul_f32_e32 v235, v43, v135
	v_mul_f32_e32 v236, v27, v135
	v_mul_f32_e32 v237, v11, v135
	v_mov_b32_dpp v238, v230 quad_perm:[1,0,3,2] row_mask:0xf bank_mask:0xf
	v_mov_b32_dpp v239, v231 quad_perm:[1,0,3,2] row_mask:0xf bank_mask:0xf
	v_mov_b32_dpp v240, v232 quad_perm:[1,0,3,2] row_mask:0xf bank_mask:0xf
	v_mov_b32_dpp v241, v233 quad_perm:[1,0,3,2] row_mask:0xf bank_mask:0xf
	v_mov_b32_dpp v242, v234 quad_perm:[1,0,3,2] row_mask:0xf bank_mask:0xf
	v_mov_b32_dpp v243, v235 quad_perm:[1,0,3,2] row_mask:0xf bank_mask:0xf
	v_mov_b32_dpp v244, v236 quad_perm:[1,0,3,2] row_mask:0xf bank_mask:0xf
; __device__ __forceinline__ int crow(int r, int hi) { return (r & 3) + 8 * (r >> 2) + 4 * hi; }
; __device__ __forceinline__ void block(const Blk& B, char* lds, A3_LAS unsigned char* ldsl, const int tid) {
;     ...
;     for (int r = 0; r < 16; ++r) { const int orow = attn::crow(r, hi);
; #pragma unroll
;         for (int d0 = 0; d0 < 8; ++d0) { const float v = o[d0][r] * rli[r]; const float vn = __shfl_xor(v, 1);
;             if ((r32 & 1) == 0) *(unsigned*)(Ow + (size_t)orow * LDO + d0 * 32 + r32) = attn::cvtpk(v, vn); } }
	v_mov_b32_dpp v245, v237 quad_perm:[1,0,3,2] row_mask:0xf bank_mask:0xf
	v_cvt_pk_bf16_f32 v230, v230, v238
	v_cvt_pk_bf16_f32 v231, v231, v239
	v_cvt_pk_bf16_f32 v232, v232, v240
	v_cvt_pk_bf16_f32 v233, v233, v241
	v_cvt_pk_bf16_f32 v234, v234, v242
	v_cvt_pk_bf16_f32 v235, v235, v243
	v_cvt_pk_bf16_f32 v236, v236, v244
	v_cvt_pk_bf16_f32 v237, v237, v245
	s_mov_b64 exec, s[2:3]
	global_store_dword v[228:229], v230, off
	global_store_dword v[228:229], v231, off offset:64
	global_store_dword v[228:229], v232, off offset:128
	global_store_dword v[228:229], v233, off offset:192
	global_store_dword v[228:229], v234, off offset:256
	global_store_dword v[228:229], v235, off offset:320
	global_store_dword v[228:229], v236, off offset:384
	global_store_dword v[228:229], v237, off offset:448
	s_mov_b64 exec, -1
	s_mov_b64 s[60:61], 0x24000
	v_lshl_add_u64 v[228:229], v[146:147], 0, s[60:61]
	v_mul_f32_e32 v212, v124, v136
	v_mul_f32_e32 v213, v108, v136
	v_mul_f32_e32 v214, v92, v136
	v_mul_f32_e32 v215, v76, v136
	v_mul_f32_e32 v216, v60, v136
	v_mul_f32_e32 v217, v44, v136
	v_mul_f32_e32 v218, v28, v136
	v_mul_f32_e32 v219, v12, v136
	v_mov_b32_dpp v220, v212 quad_perm:[1,0,3,2] row_mask:0xf bank_mask:0xf
	v_mov_b32_dpp v221, v213 quad_perm:[1,0,3,2] row_mask:0xf bank_mask:0xf
	v_mov_b32_dpp v222, v214 quad_perm:[1,0,3,2] row_mask:0xf bank_mask:0xf
	v_mov_b32_dpp v223, v215 quad_perm:[1,0,3,2] row_mask:0xf bank_mask:0xf
	v_mov_b32_dpp v224, v216 quad_perm:[1,0,3,2] row_mask:0xf bank_mask:0xf
	v_mov_b32_dpp v225, v217 quad_perm:[1,0,3,2] row_mask:0xf bank_mask:0xf
	v_mov_b32_dpp v226, v218 quad_perm:[1,0,3,2] row_mask:0xf bank_mask:0xf
	v_mov_b32_dpp v227, v219 quad_perm:[1,0,3,2] row_mask:0xf bank_mask:0xf
	v_cvt_pk_bf16_f32 v212, v212, v220
	v_cvt_pk_bf16_f32 v213, v213, v221
	v_cvt_pk_bf16_f32 v214, v214, v222
	v_cvt_pk_bf16_f32 v215, v215, v223
	v_cvt_pk_bf16_f32 v216, v216, v224
	v_cvt_pk_bf16_f32 v217, v217, v225
	v_cvt_pk_bf16_f32 v218, v218, v226
	v_cvt_pk_bf16_f32 v219, v219, v227
	s_mov_b64 exec, s[2:3]
	global_store_dword v[228:229], v212, off
	global_store_dword v[228:229], v213, off offset:64
	global_store_dword v[228:229], v214, off offset:128
	global_store_dword v[228:229], v215, off offset:192
	global_store_dword v[228:229], v216, off offset:256
	global_store_dword v[228:229], v217, off offset:320
	global_store_dword v[228:229], v218, off offset:384
	global_store_dword v[228:229], v219, off offset:448
	s_mov_b64 exec, -1
	s_mov_b64 s[60:61], 0x26000
	v_lshl_add_u64 v[228:229], v[146:147], 0, s[60:61]
	v_mul_f32_e32 v230, v125, v137
	v_mul_f32_e32 v231, v109, v137
	v_mul_f32_e32 v232, v93, v137
	v_mul_f32_e32 v233, v77, v137
	v_mul_f32_e32 v234, v61, v137
	v_mul_f32_e32 v235, v45, v137
	v_mul_f32_e32 v236, v29, v137
	v_mul_f32_e32 v237, v13, v137
	v_mov_b32_dpp v238, v230 quad_perm:[1,0,3,2] row_mask:0xf bank_mask:0xf
	v_mov_b32_dpp v239, v231 quad_perm:[1,0,3,2] row_mask:0xf bank_mask:0xf
	v_mov_b32_dpp v240, v232 quad_perm:[1,0,3,2] row_mask:0xf bank_mask:0xf
	v_mov_b32_dpp v241, v233 quad_perm:[1,0,3,2] row_mask:0xf bank_mask:0xf
	v_mov_b32_dpp v242, v234 quad_perm:[1,0,3,2] row_mask:0xf bank_mask:0xf
	v_mov_b32_dpp v243, v235 quad_perm:[1,0,3,2] row_mask:0xf bank_mask:0xf
	v_mov_b32_dpp v244, v236 quad_perm:[1,0,3,2] row_mask:0xf bank_mask:0xf
	v_mov_b32_dpp v245, v237 quad_perm:[1,0,3,2] row_mask:0xf bank_mask:0xf
	v_cvt_pk_bf16_f32 v230, v230, v238
	v_cvt_pk_bf16_f32 v231, v231, v239
	v_cvt_pk_bf16_f32 v232, v232, v240
	v_cvt_pk_bf16_f32 v233, v233, v241
	v_cvt_pk_bf16_f32 v234, v234, v242
	v_cvt_pk_bf16_f32 v235, v235, v243
	v_cvt_pk_bf16_f32 v236, v236, v244
	v_cvt_pk_bf16_f32 v237, v237, v245
	s_mov_b64 exec, s[2:3]
	global_store_dword v[228:229], v230, off
	global_store_dword v[228:229], v231, off offset:64
	global_store_dword v[228:229], v232, off offset:128
	global_store_dword v[228:229], v233, off offset:192
	global_store_dword v[228:229], v234, off offset:256
	global_store_dword v[228:229], v235, off offset:320
	global_store_dword v[228:229], v236, off offset:384
	global_store_dword v[228:229], v237, off offset:448
	s_mov_b64 exec, -1
	s_mov_b64 s[60:61], 0x30000
	v_lshl_add_u64 v[228:229], v[146:147], 0, s[60:61]
	v_mul_f32_e32 v212, v126, v130
	v_mul_f32_e32 v213, v110, v130
	v_mul_f32_e32 v214, v94, v130
	v_mul_f32_e32 v215, v78, v130
	v_mul_f32_e32 v216, v62, v130
	v_mul_f32_e32 v217, v46, v130
	v_mul_f32_e32 v218, v30, v130
	v_mul_f32_e32 v219, v14, v130
	v_mov_b32_dpp v220, v212 quad_perm:[1,0,3,2] row_mask:0xf bank_mask:0xf
	v_mov_b32_dpp v221, v213 quad_perm:[1,0,3,2] row_mask:0xf bank_mask:0xf
	v_mov_b32_dpp v222, v214 quad_perm:[1,0,3,2] row_mask:0xf bank_mask:0xf
	v_mov_b32_dpp v223, v215 quad_perm:[1,0,3,2] row_mask:0xf bank_mask:0xf
	v_mov_b32_dpp v224, v216 quad_perm:[1,0,3,2] row_mask:0xf bank_mask:0xf
	v_mov_b32_dpp v225, v217 quad_perm:[1,0,3,2] row_mask:0xf bank_mask:0xf
	v_mov_b32_dpp v226, v218 quad_perm:[1,0,3,2] row_mask:0xf bank_mask:0xf
	v_mov_b32_dpp v227, v219 quad_perm:[1,0,3,2] row_mask:0xf bank_mask:0xf
	v_cvt_pk_bf16_f32 v212, v212, v220
	v_cvt_pk_bf16_f32 v213, v213, v221
	v_cvt_pk_bf16_f32 v214, v214, v222
	v_cvt_pk_bf16_f32 v215, v215, v223
	v_cvt_pk_bf16_f32 v216, v216, v224
	v_cvt_pk_bf16_f32 v217, v217, v225
	v_cvt_pk_bf16_f32 v218, v218, v226
	v_cvt_pk_bf16_f32 v219, v219, v227
	s_mov_b64 exec, s[2:3]
	global_store_dword v[228:229], v212, off
	global_store_dword v[228:229], v213, off offset:64
	global_store_dword v[228:229], v214, off offset:128
	global_store_dword v[228:229], v215, off offset:192
	global_store_dword v[228:229], v216, off offset:256
; __device__ __forceinline__ int crow(int r, int hi) { return (r & 3) + 8 * (r >> 2) + 4 * hi; }
; __device__ __forceinline__ void block(const Blk& B, char* lds, A3_LAS unsigned char* ldsl, const int tid) {
;     ...
;     for (int r = 0; r < 16; ++r) { const int orow = attn::crow(r, hi);
; #pragma unroll
;         for (int d0 = 0; d0 < 8; ++d0) { const float v = o[d0][r] * rli[r]; const float vn = __shfl_xor(v, 1);
;             if ((r32 & 1) == 0) *(unsigned*)(Ow + (size_t)orow * LDO + d0 * 32 + r32) = attn::cvtpk(v, vn); } }
;     __syncthreads();
	global_store_dword v[228:229], v217, off offset:320
	global_store_dword v[228:229], v218, off offset:384
	global_store_dword v[228:229], v219, off offset:448
	s_mov_b64 exec, -1
	s_mov_b64 s[60:61], 0x32000
	v_lshl_add_u64 v[228:229], v[146:147], 0, s[60:61]
	v_mul_f32_e32 v230, v127, v131
	v_mul_f32_e32 v231, v111, v131
	v_mul_f32_e32 v232, v95, v131
	v_mul_f32_e32 v233, v79, v131
	v_mul_f32_e32 v234, v63, v131
	v_mul_f32_e32 v235, v47, v131
	v_mul_f32_e32 v236, v31, v131
	v_mul_f32_e32 v237, v15, v131
	v_mov_b32_dpp v238, v230 quad_perm:[1,0,3,2] row_mask:0xf bank_mask:0xf
	v_mov_b32_dpp v239, v231 quad_perm:[1,0,3,2] row_mask:0xf bank_mask:0xf
	v_mov_b32_dpp v240, v232 quad_perm:[1,0,3,2] row_mask:0xf bank_mask:0xf
	v_mov_b32_dpp v241, v233 quad_perm:[1,0,3,2] row_mask:0xf bank_mask:0xf
	v_mov_b32_dpp v242, v234 quad_perm:[1,0,3,2] row_mask:0xf bank_mask:0xf
	v_mov_b32_dpp v243, v235 quad_perm:[1,0,3,2] row_mask:0xf bank_mask:0xf
	v_mov_b32_dpp v244, v236 quad_perm:[1,0,3,2] row_mask:0xf bank_mask:0xf
	v_mov_b32_dpp v245, v237 quad_perm:[1,0,3,2] row_mask:0xf bank_mask:0xf
	v_cvt_pk_bf16_f32 v230, v230, v238
	v_cvt_pk_bf16_f32 v231, v231, v239
	v_cvt_pk_bf16_f32 v232, v232, v240
	v_cvt_pk_bf16_f32 v233, v233, v241
	v_cvt_pk_bf16_f32 v234, v234, v242
	v_cvt_pk_bf16_f32 v235, v235, v243
	v_cvt_pk_bf16_f32 v236, v236, v244
	v_cvt_pk_bf16_f32 v237, v237, v245
	s_mov_b64 exec, s[2:3]
	global_store_dword v[228:229], v230, off
	global_store_dword v[228:229], v231, off offset:64
	global_store_dword v[228:229], v232, off offset:128
	global_store_dword v[228:229], v233, off offset:192
	global_store_dword v[228:229], v234, off offset:256
	global_store_dword v[228:229], v235, off offset:320
	global_store_dword v[228:229], v236, off offset:384
	global_store_dword v[228:229], v237, off offset:448
	s_mov_b64 exec, -1
	s_mov_b64 s[60:61], 0x34000
	v_lshl_add_u64 v[228:229], v[146:147], 0, s[60:61]
	v_mul_f32_e32 v212, v128, v132
	v_mul_f32_e32 v213, v112, v132
	v_mul_f32_e32 v214, v96, v132
	v_mul_f32_e32 v215, v80, v132
	v_mul_f32_e32 v216, v64, v132
	v_mul_f32_e32 v217, v48, v132
	v_mul_f32_e32 v218, v32, v132
	v_mul_f32_e32 v219, v16, v132
	v_mov_b32_dpp v220, v212 quad_perm:[1,0,3,2] row_mask:0xf bank_mask:0xf
	v_mov_b32_dpp v221, v213 quad_perm:[1,0,3,2] row_mask:0xf bank_mask:0xf
	v_mov_b32_dpp v222, v214 quad_perm:[1,0,3,2] row_mask:0xf bank_mask:0xf
	v_mov_b32_dpp v223, v215 quad_perm:[1,0,3,2] row_mask:0xf bank_mask:0xf
	v_mov_b32_dpp v224, v216 quad_perm:[1,0,3,2] row_mask:0xf bank_mask:0xf
	v_mov_b32_dpp v225, v217 quad_perm:[1,0,3,2] row_mask:0xf bank_mask:0xf
	v_mov_b32_dpp v226, v218 quad_perm:[1,0,3,2] row_mask:0xf bank_mask:0xf
	v_mov_b32_dpp v227, v219 quad_perm:[1,0,3,2] row_mask:0xf bank_mask:0xf
	v_cvt_pk_bf16_f32 v212, v212, v220
	v_cvt_pk_bf16_f32 v213, v213, v221
	v_cvt_pk_bf16_f32 v214, v214, v222
	v_cvt_pk_bf16_f32 v215, v215, v223
	v_cvt_pk_bf16_f32 v216, v216, v224
	v_cvt_pk_bf16_f32 v217, v217, v225
	v_cvt_pk_bf16_f32 v218, v218, v226
	v_cvt_pk_bf16_f32 v219, v219, v227
	s_mov_b64 exec, s[2:3]
	global_store_dword v[228:229], v212, off
	global_store_dword v[228:229], v213, off offset:64
	global_store_dword v[228:229], v214, off offset:128
	global_store_dword v[228:229], v215, off offset:192
	global_store_dword v[228:229], v216, off offset:256
	global_store_dword v[228:229], v217, off offset:320
	global_store_dword v[228:229], v218, off offset:384
	global_store_dword v[228:229], v219, off offset:448
	s_mov_b64 exec, -1
	s_mov_b64 s[60:61], 0x36000
	v_lshl_add_u64 v[228:229], v[146:147], 0, s[60:61]
	v_mul_f32_e32 v230, v129, v133
	v_mul_f32_e32 v231, v113, v133
	v_mul_f32_e32 v232, v97, v133
	v_mul_f32_e32 v233, v81, v133
	v_mul_f32_e32 v234, v65, v133
	v_mul_f32_e32 v235, v49, v133
	v_mul_f32_e32 v236, v33, v133
	v_mul_f32_e32 v237, v17, v133
	v_mov_b32_dpp v238, v230 quad_perm:[1,0,3,2] row_mask:0xf bank_mask:0xf
	v_mov_b32_dpp v239, v231 quad_perm:[1,0,3,2] row_mask:0xf bank_mask:0xf
	v_mov_b32_dpp v240, v232 quad_perm:[1,0,3,2] row_mask:0xf bank_mask:0xf
	v_mov_b32_dpp v241, v233 quad_perm:[1,0,3,2] row_mask:0xf bank_mask:0xf
	v_mov_b32_dpp v242, v234 quad_perm:[1,0,3,2] row_mask:0xf bank_mask:0xf
	v_mov_b32_dpp v243, v235 quad_perm:[1,0,3,2] row_mask:0xf bank_mask:0xf
	v_mov_b32_dpp v244, v236 quad_perm:[1,0,3,2] row_mask:0xf bank_mask:0xf
	v_mov_b32_dpp v245, v237 quad_perm:[1,0,3,2] row_mask:0xf bank_mask:0xf
	v_cvt_pk_bf16_f32 v230, v230, v238
	v_cvt_pk_bf16_f32 v231, v231, v239
	v_cvt_pk_bf16_f32 v232, v232, v240
	v_cvt_pk_bf16_f32 v233, v233, v241
	v_cvt_pk_bf16_f32 v234, v234, v242
	v_cvt_pk_bf16_f32 v235, v235, v243
	v_cvt_pk_bf16_f32 v236, v236, v244
	v_cvt_pk_bf16_f32 v237, v237, v245
	s_mov_b64 exec, s[2:3]
	global_store_dword v[228:229], v230, off
	global_store_dword v[228:229], v231, off offset:64
	global_store_dword v[228:229], v232, off offset:128
	global_store_dword v[228:229], v233, off offset:192
	global_store_dword v[228:229], v234, off offset:256
	global_store_dword v[228:229], v235, off offset:320
	global_store_dword v[228:229], v236, off offset:384
	global_store_dword v[228:229], v237, off offset:448
	s_mov_b64 exec, -1
	s_andn2_b64 vcc, exec, s[54:55]
	s_mov_b64 s[2:3], -1
	s_waitcnt lgkmcnt(0)
	s_barrier
	s_cbranch_vccnz .LBB0_322
	s_mov_b64 s[2:3], s[0:1]
	s_andn2_b64 vcc, exec, s[8:9]
	v_mbcnt_lo_u32_b32 v66, -1, 0
	v_mbcnt_hi_u32_b32 v66, -1, v66
	s_cbranch_vccnz .LBB0_321
	s_mov_b64 s[58:59], -1
	s_and_b64 vcc, exec, s[10:11]
	s_cbranch_vccz .LBB0_611
	s_and_b64 vcc, exec, s[12:13]
	s_cbranch_vccz .LBB0_608
	s_and_b64 vcc, exec, s[14:15]
	s_cbranch_vccz .LBB0_606
	s_mov_b64 s[54:55], -1
	s_and_b64 vcc, exec, s[26:27]
	s_cbranch_vccz .LBB0_603
	s_load_dwordx2 s[4:5], s[2:3], 0x98
	s_mov_b64 s[54:55], 0
	s_waitcnt lgkmcnt(0)
	s_add_u32 s56, s4, s30
	s_addc_u32 s57, s5, s31
